# static s_setprio 1 for the work-heavier wave half (waves 0-3, five value tiles) during the mLSTM output unit
# speedup vs baseline: 1.0056x; 1.0056x over previous
; #define FRESH() const int tid = TID(), lane = tid & 63, wave = __builtin_amdgcn_readfirstlane(tid >> 6); (void)lane; (void)wave
; #define PH(k, ...) if (IN(k)) { _Pragma("unroll") for (int rep_ = 0; rep_ < ((DUP_PHASE) == (k) ? 2 : 1); ++rep_) { if (rep_) xcd_barrier(bar, TID()); __VA_ARGS__ } } SEAM(k);
; __device__ __forceinline__ void ml_out_unit(const Args& a, unsigned char* lds_g, int u, int tid) {
;     const int L = u & 7, h = (u >> 3) & 7, b = u >> 6;
;     const int rowbase = NCTX + b * SEQ + 256 * L;
;     const int lane = tid & 63, w = __builtin_amdgcn_readfirstlane(tid >> 6), fr = lane & 15, fq = lane >> 4;
;     bf16* CB = (bf16*)(lds_g + ML_CB);
;     ml_gates(a, lds_g, rowbase, h, tid);
;     f32x4 st[9];
; #pragma unroll
;     for (int dir = 0; dir < 2; ++dir) {
;         const int seq = (b * 8 + h) * 2 + dir, jmax = dir ? 7 - L : L;
;         const float* BT = (const float*)(a.ws + WS_BT) + seq * 8;
; __global__ void __launch_bounds__(NTHR, 2) fwd_kernel(Args args) {
;     ...
;     PH(3, { FRESH();
;         for (int u = c; u < 256; u += G) ml_out_unit(args, lds, u, tid);
.Lp3_ml:
	s_cmpk_gt_i32 s83, 0xff
	v_mbcnt_lo_u32_b32 v4, -1, 0
	v_mbcnt_hi_u32_b32 v4, -1, v4
	s_nop 0
	s_nop 0
	s_nop 0
	v_readlane_b32 s0, v249, 1
	s_nop 1
	v_or_b32_e32 v113, s0, v4
	s_cbranch_scc1 .LBB0_667
	v_readfirstlane_b32 s0, v113
	s_cmpk_lt_u32 s0, 0x100
	s_cbranch_scc0 .Lmlp_skip
	s_setprio 1
.Lmlp_skip:
	s_add_u32 s0, s84, 0x200000
	s_addc_u32 s1, s85, 0
	v_writelane_b32 v249, s0, 26
	v_lshlrev_b32_e32 v10, 3, v4
	v_and_b32_e32 v10, 24, v10
	v_writelane_b32 v249, s1, 27
	s_add_u32 s0, s84, 0x3d600000
	v_writelane_b32 v249, s0, 28
	s_addc_u32 s0, s85, 0
	s_add_u32 s72, s84, 0x1ec00000
	s_addc_u32 s73, s85, 0
	s_add_u32 s46, s84, 0x22200000
	s_addc_u32 s47, s85, 0
	s_add_u32 s2, s84, 0x1fe00000
	s_addc_u32 s3, s85, 0
	s_add_u32 s54, s84, 0x37200000
	s_addc_u32 s55, s85, 0
	s_waitcnt lgkmcnt(0)
	s_add_u32 s56, s84, 0x24200000
	s_addc_u32 s57, s85, 0
	v_writelane_b32 v249, s0, 29
	s_add_u32 s0, s84, 0x3b200000
	v_lshrrev_b32_e32 v133, 3, v113
	v_add_u32_e32 v149, 0, v10
	v_lshrrev_b32_e32 v10, 1, v4
	v_writelane_b32 v249, s0, 30
	s_addc_u32 s0, s85, 0
	v_and_b32_e32 v112, 15, v4
	v_lshrrev_b32_e32 v1, 2, v113
	v_lshrrev_b32_e32 v0, 1, v113
	v_and_b32_e32 v7, 7, v4
	v_mul_u32_u24_e32 v2, 0x88, v133
	v_and_b32_e32 v10, 24, v10
	v_writelane_b32 v249, s0, 31
	v_mov_b32_e32 v5, 0
	v_and_b32_e32 v3, 24, v0
	v_lshrrev_b32_e32 v6, 4, v4
	v_lshlrev_b32_e32 v0, 4, v7
	v_lshl_add_u32 v8, v2, 1, 0
	v_lshlrev_b32_e32 v2, 5, v7
	v_cmp_eq_u32_e64 s[36:37], 0, v7
	v_lshrrev_b32_e32 v7, 2, v4
	s_add_i32 s1, 0, 0x17d40
	v_and_or_b32 v1, v1, 3, v10
	s_movk_i32 s50, 0x110
	v_mul_u32_u24_e32 v10, 0x110, v112
	v_lshlrev_b32_e32 v135, 2, v6
	s_movk_i32 s0, 0x88
	v_and_b32_e32 v150, -16, v4
	v_writelane_b32 v249, s1, 32
	v_lshlrev_b32_e32 v6, 3, v6
	v_mad_u32_u24 v153, v7, s50, v149
	v_lshlrev_b32_e32 v154, 5, v7
	v_mov_b32_e32 v7, 0x1100
	v_add3_u32 v162, 0, v3, v10
	v_mov_b32_e32 v3, v5
	v_add_u32_e32 v146, v8, v2
	v_add_u32_e32 v151, s1, v150
	v_mad_u32_u24 v159, v1, s0, v7
	v_add3_u32 v161, 0, v6, v10
	v_lshl_add_u64 v[6:7], v[4:5], 3, s[84:85]
	s_mov_b64 s[0:1], 0x3d800000
	v_lshl_add_u64 v[116:117], s[72:73], 0, v[2:3]
	v_writelane_b32 v249, s2, 33
	v_lshl_add_u64 v[114:115], v[6:7], 0, s[0:1]
	s_mov_b64 s[0:1], 0x23200000
	v_lshl_add_u64 v[118:119], s[2:3], 0, v[2:3]
	v_lshlrev_b32_e32 v2, 1, v112
	v_writelane_b32 v249, s3, 34
	v_lshl_add_u64 v[2:3], s[84:85], 0, v[2:3]
	v_cmp_eq_u32_e64 s[4:5], 0, v112
	v_lshl_add_u64 v[120:121], v[2:3], 0, s[0:1]
	v_readlane_b32 s0, v249, 1
	v_and_b32_e32 v147, 48, v4
	v_add_u32_e32 v148, 0, v147
	v_add_u32_e32 v2, s0, v4
	s_xor_b64 s[0:1], s[4:5], -1
	v_writelane_b32 v249, s0, 35
	v_lshrrev_b32_e32 v2, 3, v2
	v_or_b32_e32 v11, 1, v135
	v_writelane_b32 v249, s1, 36
	v_lshlrev_b32_e32 v158, 5, v1
	v_lshlrev_b32_e32 v3, 2, v2
	v_lshlrev_b32_e32 v122, 1, v0
	v_mbcnt_lo_u32_b32 v0, -1, 0
	v_writelane_b32 v249, s96, 37
	v_mul_i32_i24_e32 v9, 0xffffff10, v133
	v_mad_u32_u24 v152, v112, s50, v148
	v_cmp_lt_u32_e64 s[8:9], v11, v112
	v_or_b32_e32 v11, 2, v135
	v_or_b32_e32 v12, 3, v135
	v_mul_u32_u24_e32 v156, 0x88, v1
	v_or_b32_e32 v1, 0x400, v158
	v_add_u32_e32 v4, 0, v3
	s_mov_b32 s62, 0xffe00000
	v_mbcnt_hi_u32_b32 v173, -1, v0
	v_mov_b32_e32 v0, 0x80
	v_writelane_b32 v249, s97, 38
	s_mov_b32 s61, 0
	v_cmp_lt_u32_e64 s[6:7], v135, v112
	v_cmp_lt_u32_e64 s[10:11], v11, v112
	v_cmp_lt_u32_e64 s[12:13], v12, v112
	v_add_u32_e32 v155, 0xd400, v152
	v_lshl_add_u32 v157, v156, 1, v149
	v_lshl_add_u32 v160, v159, 1, v149
	v_cmp_gt_u32_e64 s[14:15], v135, v112
	v_cmp_gt_u32_e64 s[16:17], v11, v112
	v_cmp_gt_u32_e64 s[18:19], v12, v112
	v_add_u32_e32 v163, 0, v150
	v_add_u32_e32 v164, 0x440, v2
	v_add_u32_e32 v165, 0x17500, v4
	v_add_u32_e32 v166, 0x480, v2
	v_add_u32_e32 v167, 0x17c00, v3
	v_mov_b32_e32 v168, 0x3ecc95a3
	v_mov_b32_e32 v169, 0x7f800000
	s_movk_i32 s49, 0x1000
	s_mov_b32 s63, -1
	s_add_i32 s2, 0, 0x17e40
	s_movk_i32 s51, 0x7fff
	v_mov_b32_e32 v170, 0x358637bd
	v_mov_b32_e32 v171, 0x7fc00000
	v_mov_b32_e32 v172, 0xff800000
	v_lshl_or_b32 v174, v173, 2, v0
	v_mov_b32_e32 v175, 0x1200
	v_add_u32_e32 v176, v8, v9
	v_mov_b32_e32 v8, v5
	v_mov_b32_e32 v9, v5
	v_mov_b32_e32 v10, v5
	v_mov_b32_e32 v11, v5
	v_add_u32_e32 v177, v149, v1
	s_mov_b32 s3, s83
	s_mov_b32 s0, s83
	v_writelane_b32 v249, s83, 39
	v_writelane_b32 v249, s82, 40
	s_branch .LBB0_369

; __device__ __forceinline__ int fresh_lane() { int l; asm volatile("v_mbcnt_lo_u32_b32 %0, -1, 0\n\tv_mbcnt_hi_u32_b32 %0, -1, %0" : "=v"(l)); __builtin_assume(l >= 0 && l < 64); return l; }
; __device__ __forceinline__ void lru_out_loadps(const Args& a, int b, int cidx, int blk, int tid, unsigned (&psw)[2][16]) {
;     const int chl = tid & 127, q = tid >> 7, ch = blk * 128 + chl;
; #pragma unroll
;     for (int d = 0; d < 2; ++d) { const unsigned* PS = (const unsigned*)(a.ws + WS_PS) + ((size_t)(b * 2 + d) * NSTEP + 64 * cidx + 16 * q) * 1024 + ch;
; #pragma unroll
;         for (int i = 0; i < 16; ++i) psw[d][i] = PS[(size_t)i * 1024]; }
; }
; __global__ void __launch_bounds__(NTHR, 2) fwd_kernel(Args args) {
;     ...
;         unsigned psw[2][16];
;         if (c < 4 * 32 * 8) { const int q = c >> 3; lru_out_loadps(args, q >> 5, 4 + (q & 31), c & 7, __builtin_amdgcn_readfirstlane(tid >> 6) * 64 + fresh_lane(), psw); }
.LBB0_667:
	s_setprio 0
	s_cmp_eq_u32 s100, 2
	s_cbranch_scc1 .LBB0_684
	v_readlane_b32 s0, v249, 24
	s_cmpk_lt_i32 s83, 0x400
	v_readlane_b32 s1, v249, 25
	s_cbranch_scc0 .LBB0_685
	s_lshl_b32 s0, s83, 7
	s_and_b32 s3, s0, 0x380
	s_waitcnt lgkmcnt(0)
	s_add_u32 s4, s84, 0x4800000
	s_addc_u32 s5, s85, 0
	s_lshl_b32 s6, s83, 3
	s_ashr_i32 s1, s83, 7
	s_and_b32 s6, s6, 0x7c0
	s_and_b32 s2, s1, -2
	s_add_i32 s10, s6, 0x100
	s_or_b32 s1, s1, 1
	s_add_u32 s6, s84, 0x25200000
	s_addc_u32 s7, s85, 0
	s_mul_hi_i32 s13, s1, 0x900
	s_mul_i32 s14, s1, 0x900
	s_add_u32 s1, s84, 0x3d200000
	s_mul_hi_i32 s11, s2, 0x900
	s_mul_i32 s12, s2, 0x900
	s_addc_u32 s2, s85, 0
	s_add_u32 s8, s84, 0x3c200000
	v_readlane_b32 s15, v249, 0
	s_addc_u32 s9, s85, 0
	s_lshr_b32 s15, s15, 6
	v_mbcnt_lo_u32_b32 v0, -1, 0
	v_mbcnt_hi_u32_b32 v0, -1, v0
	s_lshl_b32 s16, s15, 6
	v_or_b32_e32 v0, s3, v0
	s_lshl_b32 s3, s15, 3
	s_and_b32 s3, s3, -16
	s_ashr_i32 s15, s3, 31
	v_and_or_b32 v64, s16, 64, v0
	s_add_u32 s16, s3, s10
	s_addc_u32 s15, s15, 0
	s_add_u32 s10, s16, s12
	v_mov_b32_e32 v65, 0
	s_addc_u32 s11, s15, s11
	v_lshl_add_u64 v[0:1], v[64:65], 2, s[4:5]
	s_lshl_b64 s[10:11], s[10:11], 12
	v_lshl_add_u64 v[2:3], v[0:1], 0, s[10:11]
	s_movk_i32 s3, 0x2000
	v_add_co_u32_e32 v4, vcc, s3, v2
	s_movk_i32 s33, 0x4000
	s_nop 0
	v_addc_co_u32_e32 v5, vcc, 0, v3, vcc
	v_add_co_u32_e32 v6, vcc, s33, v2
	s_movk_i32 s38, 0x6000
	s_nop 0
	v_addc_co_u32_e32 v7, vcc, 0, v3, vcc
	v_add_co_u32_e32 v8, vcc, s38, v2
	s_mov_b32 s39, 0x8000
	s_nop 0
	v_addc_co_u32_e32 v9, vcc, 0, v3, vcc
	v_add_co_u32_e32 v10, vcc, s39, v2
	s_mov_b32 s44, 0xa000
	s_nop 0
	v_addc_co_u32_e32 v11, vcc, 0, v3, vcc
	s_waitcnt vmcnt(0)
	v_add_co_u32_e32 v12, vcc, s44, v2
	s_mov_b32 s45, 0xc000
	s_nop 0
	v_addc_co_u32_e32 v13, vcc, 0, v3, vcc
	v_add_co_u32_e32 v14, vcc, s45, v2
	s_mov_b32 s50, 0xe000
	s_nop 0
	v_addc_co_u32_e32 v15, vcc, 0, v3, vcc
	global_load_dword v37, v[8:9], off offset:-4096
	global_load_dword v38, v[8:9], off
	global_load_dword v39, v[10:11], off offset:-4096
	global_load_dword v40, v[10:11], off
	global_load_dword v41, v[12:13], off offset:-4096
	global_load_dword v42, v[12:13], off
	global_load_dword v43, v[14:15], off offset:-4096
	global_load_dword v44, v[14:15], off
	v_add_co_u32_e32 v8, vcc, s50, v2
	s_add_u32 s10, s16, s14
	s_nop 0
	v_addc_co_u32_e32 v9, vcc, 0, v3, vcc
	s_mov_b32 s51, 0xf000
	s_addc_u32 s11, s15, s13
	v_add_co_u32_e32 v10, vcc, s51, v2
	s_lshl_b64 s[10:11], s[10:11], 12
	s_nop 0
	v_addc_co_u32_e32 v11, vcc, 0, v3, vcc
	v_lshl_add_u64 v[0:1], v[0:1], 0, s[10:11]
	v_add_co_u32_e32 v12, vcc, s3, v0
	s_lshl_b32 s72, s82, 7
	s_nop 0
	v_addc_co_u32_e32 v13, vcc, 0, v1, vcc
	v_add_co_u32_e32 v14, vcc, s33, v0
	s_movk_i32 s73, 0x7fff
	s_nop 0
	v_addc_co_u32_e32 v15, vcc, 0, v1, vcc
	v_add_co_u32_e32 v16, vcc, s38, v0
	s_mov_b32 s74, s83
	s_nop 0
	v_addc_co_u32_e32 v17, vcc, 0, v1, vcc
	global_load_dword v45, v[8:9], off offset:-4096
	global_load_dword v46, v[8:9], off
	global_load_dword v49, v[12:13], off offset:-4096
	global_load_dword v50, v[12:13], off
	global_load_dword v51, v[14:15], off offset:-4096
	global_load_dword v52, v[14:15], off
	global_load_dword v53, v[16:17], off offset:-4096
	global_load_dword v54, v[16:17], off
	v_add_co_u32_e32 v8, vcc, s39, v0
	s_nop 1
	v_addc_co_u32_e32 v9, vcc, 0, v1, vcc
	v_add_co_u32_e32 v12, vcc, s44, v0
	s_nop 1
	v_addc_co_u32_e32 v13, vcc, 0, v1, vcc
	v_add_co_u32_e32 v14, vcc, s45, v0
	s_nop 1
	v_addc_co_u32_e32 v15, vcc, 0, v1, vcc
	v_add_co_u32_e32 v16, vcc, s50, v0
	s_nop 1
	v_addc_co_u32_e32 v17, vcc, 0, v1, vcc
	global_load_dword v55, v[8:9], off offset:-4096
	global_load_dword v56, v[8:9], off
	global_load_dword v57, v[12:13], off offset:-4096
	global_load_dword v58, v[12:13], off
	global_load_dword v59, v[14:15], off offset:-4096
	global_load_dword v60, v[14:15], off
	global_load_dword v61, v[16:17], off offset:-4096
	global_load_dword v62, v[16:17], off
	v_add_co_u32_e32 v8, vcc, s51, v0
	s_nop 1
	v_addc_co_u32_e32 v9, vcc, 0, v1, vcc
	global_load_dword v32, v[2:3], off
	global_load_dword v33, v[4:5], off offset:-4096
	global_load_dword v34, v[4:5], off
	global_load_dword v35, v[6:7], off offset:-4096
	global_load_dword v36, v[6:7], off
	global_load_dword v47, v[10:11], off
	global_load_dword v48, v[0:1], off
	global_load_dword v63, v[8:9], off
	s_waitcnt vmcnt(0)
	v_mov_b64_e32 v[0:1], v[32:33]
	v_mov_b64_e32 v[2:3], v[34:35]
	v_mov_b64_e32 v[4:5], v[36:37]
	v_mov_b64_e32 v[6:7], v[38:39]
	v_mov_b64_e32 v[8:9], v[40:41]
	v_mov_b64_e32 v[10:11], v[42:43]
	v_mov_b64_e32 v[12:13], v[44:45]
	v_mov_b64_e32 v[14:15], v[46:47]
	v_mov_b64_e32 v[16:17], v[48:49]
	v_mov_b64_e32 v[18:19], v[50:51]
	v_mov_b64_e32 v[20:21], v[52:53]
	v_mov_b64_e32 v[22:23], v[54:55]
	v_mov_b64_e32 v[24:25], v[56:57]
	v_mov_b64_e32 v[26:27], v[58:59]
	v_mov_b64_e32 v[28:29], v[60:61]
	v_mov_b64_e32 v[30:31], v[62:63]
	s_branch .LBB0_670
